# speedup vs baseline: 1.0209x; 1.0048x over previous
.LBB1_4:
	s_and_b64 s[0:1], s[62:63], exec
	v_readlane_b32 s0, v248, 14
	s_cselect_b32 s83, s0, s70
	s_lshl_b32 s90, s83, 7
	s_lshl_b32 s89, s88, 5
	v_and_b32_e32 v167, 31, v55
	v_lshrrev_b32_e32 v5, 5, v165
	s_ashr_i32 s91, s95, 8
	s_or_b32 s93, s89, s90
	v_or_b32_e32 v6, s93, v167
	v_lshlrev_b32_e32 v168, 2, v5
	s_lshl_b32 s64, s91, 14
	v_sub_u32_e32 v171, v6, v168
	s_add_i32 s0, s64, 0
	s_add_i32 s0, s0, 0x10000
	s_barrier
	v_lshlrev_b32_e32 v53, 8, v167
	v_lshlrev_b32_e32 v61, 4, v5
	v_and_b32_e32 v86, 0xf0, v4
	v_bitop3_b32 v4, v61, v53, v86 bitop3:0xde
	v_add_u32_e32 v172, s0, v4
	v_xor_b32_e32 v249, 0x80, v172
	ds_read_b128 v[4:7], v172
	ds_read_b128 v[62:65], v249
	v_or_b32_e32 v8, 32, v61
	s_waitcnt lgkmcnt(0)
	v_mfma_f32_32x32x16_f16 v[20:35], v[4:7], v[114:117], 0
	ds_read_b128 v[4:7], v172 offset:8192
	ds_read_b128 v[66:69], v249 offset:8192
	v_bitop3_b32 v8, v8, v53, v86 bitop3:0xde
	v_add_u32_e32 v173, s0, v8
	v_xor_b32_e32 v253, 0x80, v173
	ds_read_b128 v[70:73], v173
	ds_read_b128 v[74:77], v253
	v_or_b32_e32 v78, 64, v61
	v_bitop3_b32 v78, v78, v53, v86 bitop3:0xde
	s_waitcnt lgkmcnt(0)
	v_mfma_f32_32x32x16_f16 v[20:35], v[70:73], v[118:121], v[20:35]
	ds_read_b128 v[70:73], v173 offset:8192
	v_add_u32_e32 v174, s0, v78
	v_xor_b32_e32 v254, 0x80, v174
	ds_read_b128 v[78:81], v253 offset:8192
	v_or_b32_e32 v61, 0x60, v61
	v_bitop3_b32 v53, v61, v53, v86 bitop3:0xde
	v_add_u32_e32 v175, s0, v53
	v_xor_b32_e32 v255, 0x80, v175
	s_lshl_b32 s82, s91, 6
	v_mfma_f32_32x32x16_f16 v[4:19], v[4:7], v[114:117], 0
	s_or_b32 s0, s82, 63
	s_cmp_le_i32 s0, s93
	v_subrev_u32_e32 v53, s82, v171
	s_waitcnt lgkmcnt(0)
	v_mfma_f32_32x32x16_f16 v[4:19], v[70:73], v[118:121], v[4:19]
	ds_read_b128 v[70:73], v174
	ds_read_b128 v[82:85], v254
	ds_read_b128 v[86:89], v254 offset:8192
	s_waitcnt lgkmcnt(0)
	v_mfma_f32_32x32x16_f16 v[20:35], v[70:73], v[122:125], v[20:35]
	ds_read_b128 v[70:73], v174 offset:8192
	s_waitcnt lgkmcnt(0)
	v_mfma_f32_32x32x16_f16 v[4:19], v[70:73], v[122:125], v[4:19]
	ds_read_b128 v[70:73], v175
	ds_read_b128 v[90:93], v255
	s_waitcnt lgkmcnt(0)
	v_mfma_f32_32x32x16_f16 v[20:35], v[70:73], v[126:129], v[20:35]
	ds_read_b128 v[70:73], v175 offset:8192
	ds_read_b128 v[94:97], v255 offset:8192
	s_waitcnt lgkmcnt(0)
	v_mfma_f32_32x32x16_f16 v[4:19], v[70:73], v[126:129], v[4:19]
	s_waitcnt vmcnt(0)
	v_mfma_f32_32x32x16_f16 v[20:35], v[62:65], v[130:133], v[20:35]
	v_mfma_f32_32x32x16_f16 v[4:19], v[66:69], v[130:133], v[4:19]
	s_waitcnt vmcnt(8)
	v_mfma_f32_32x32x16_f16 v[20:35], v[74:77], v[134:137], v[20:35]
	v_mfma_f32_32x32x16_f16 v[4:19], v[78:81], v[134:137], v[4:19]
	s_waitcnt vmcnt(7)
	v_mfma_f32_32x32x16_f16 v[20:35], v[82:85], v[138:141], v[20:35]
	v_mfma_f32_32x32x16_f16 v[4:19], v[86:89], v[138:141], v[4:19]
	s_waitcnt vmcnt(6)
	v_mfma_f32_32x32x16_f16 v[20:35], v[90:93], v[142:145], v[20:35]
	s_waitcnt lgkmcnt(0)
	v_mfma_f32_32x32x16_f16 v[4:19], v[94:97], v[142:145], v[4:19]
	s_cbranch_scc1 .LBB1_6
	v_cmp_gt_i32_e64 s[58:59], 26, v53
	v_cmp_gt_i32_e64 s[60:61], 27, v53
	v_cmp_gt_i32_e64 s[56:57], 25, v53
	s_and_b64 s[58:59], s[60:61], s[58:59]
	v_cmp_gt_i32_e64 s[54:55], 24, v53
	s_and_b64 s[56:57], s[58:59], s[56:57]
	v_cmp_gt_i32_e64 s[52:53], 19, v53
	s_and_b64 s[54:55], s[56:57], s[54:55]
	v_cmp_gt_i32_e64 s[50:51], 18, v53
	s_and_b64 s[52:53], s[54:55], s[52:53]
	v_cmp_gt_i32_e64 s[48:49], 17, v53
	s_and_b64 s[50:51], s[52:53], s[50:51]
	v_cmp_gt_i32_e64 s[46:47], 16, v53
	s_and_b64 s[48:49], s[50:51], s[48:49]
	v_cmp_gt_i32_e64 s[44:45], 11, v53
	s_and_b64 s[46:47], s[48:49], s[46:47]
	v_cmp_gt_i32_e64 s[42:43], 10, v53
	s_and_b64 s[44:45], s[46:47], s[44:45]
	v_cmp_gt_i32_e64 s[40:41], 9, v53
	s_and_b64 s[42:43], s[44:45], s[42:43]
	v_cmp_gt_i32_e64 s[38:39], 8, v53
	s_and_b64 s[40:41], s[42:43], s[40:41]
	v_cmp_gt_i32_e64 s[36:37], 3, v53
	s_and_b64 s[38:39], s[40:41], s[38:39]
	v_cmp_gt_i32_e64 s[34:35], 2, v53
	s_and_b64 s[36:37], s[38:39], s[36:37]
	v_cmp_gt_i32_e64 s[30:31], 1, v53
	s_and_b64 s[34:35], s[36:37], s[34:35]
	v_cmp_gt_i32_e64 s[28:29], 0, v53
	s_and_b64 s[30:31], s[34:35], s[30:31]
	s_and_b64 s[28:29], s[30:31], s[28:29]
	v_cmp_gt_i32_e64 s[26:27], 58, v53
	v_cndmask_b32_e64 v20, v20, v164, s[28:29]
	v_cmp_gt_i32_e64 s[28:29], 59, v53
	v_cmp_gt_i32_e64 s[24:25], 57, v53
	s_and_b64 s[26:27], s[28:29], s[26:27]
	v_cmp_gt_i32_e64 s[22:23], 56, v53
	s_and_b64 s[24:25], s[26:27], s[24:25]
	v_cmp_gt_i32_e64 s[20:21], 51, v53
	s_and_b64 s[22:23], s[24:25], s[22:23]
	v_cmp_gt_i32_e64 s[18:19], 50, v53
	s_and_b64 s[20:21], s[22:23], s[20:21]
	v_cmp_gt_i32_e64 s[16:17], 49, v53
	s_and_b64 s[18:19], s[20:21], s[18:19]
	v_cmp_gt_i32_e64 s[14:15], 48, v53
	s_and_b64 s[16:17], s[18:19], s[16:17]
	v_cmp_gt_i32_e64 s[12:13], 43, v53
	s_and_b64 s[14:15], s[16:17], s[14:15]
	v_cmp_gt_i32_e64 s[10:11], 42, v53
	s_and_b64 s[12:13], s[14:15], s[12:13]
	v_cmp_gt_i32_e64 s[8:9], 41, v53
	s_and_b64 s[10:11], s[12:13], s[10:11]
	v_cmp_gt_i32_e64 s[6:7], 40, v53
	s_and_b64 s[8:9], s[10:11], s[8:9]
	v_cmp_gt_i32_e64 s[4:5], 35, v53
	s_and_b64 s[6:7], s[8:9], s[6:7]
	v_cmp_gt_i32_e64 s[2:3], 34, v53
	s_and_b64 s[4:5], s[6:7], s[4:5]
	v_cmp_gt_i32_e64 s[0:1], 33, v53
	s_and_b64 s[2:3], s[4:5], s[2:3]
	v_cmp_gt_i32_e32 vcc, 32, v53
	s_and_b64 s[0:1], s[2:3], s[0:1]
	s_and_b64 vcc, s[0:1], vcc
	v_cndmask_b32_e64 v35, v35, v164, s[60:61]
	v_cndmask_b32_e64 v34, v34, v164, s[58:59]
	v_cndmask_b32_e64 v33, v33, v164, s[56:57]
	v_cndmask_b32_e64 v32, v32, v164, s[54:55]
	v_cndmask_b32_e64 v31, v31, v164, s[52:53]
	v_cndmask_b32_e64 v30, v30, v164, s[50:51]
	v_cndmask_b32_e64 v29, v29, v164, s[48:49]
	v_cndmask_b32_e64 v28, v28, v164, s[46:47]
	v_cndmask_b32_e64 v27, v27, v164, s[44:45]
	v_cndmask_b32_e64 v26, v26, v164, s[42:43]
	v_cndmask_b32_e64 v25, v25, v164, s[40:41]
	v_cndmask_b32_e64 v24, v24, v164, s[38:39]
	v_cndmask_b32_e64 v23, v23, v164, s[36:37]
	v_cndmask_b32_e64 v22, v22, v164, s[34:35]
	v_cndmask_b32_e64 v21, v21, v164, s[30:31]
	v_cndmask_b32_e64 v19, v19, v164, s[28:29]
	v_cndmask_b32_e64 v18, v18, v164, s[26:27]
	v_cndmask_b32_e64 v17, v17, v164, s[24:25]
	v_cndmask_b32_e64 v16, v16, v164, s[22:23]
	v_cndmask_b32_e64 v15, v15, v164, s[20:21]
	v_cndmask_b32_e64 v14, v14, v164, s[18:19]
	v_cndmask_b32_e64 v13, v13, v164, s[16:17]
	v_cndmask_b32_e64 v12, v12, v164, s[14:15]
	v_cndmask_b32_e64 v11, v11, v164, s[12:13]
	v_cndmask_b32_e64 v10, v10, v164, s[10:11]
	v_cndmask_b32_e64 v9, v9, v164, s[8:9]
	v_cndmask_b32_e64 v8, v8, v164, s[6:7]
	v_cndmask_b32_e64 v7, v7, v164, s[4:5]
	v_cndmask_b32_e64 v6, v6, v164, s[2:3]
	v_cndmask_b32_e64 v5, v5, v164, s[0:1]
	v_cndmask_b32_e32 v4, v4, v164, vcc

.LBB1_12:
	ds_read_b128 v[4:7], v172 offset:32768
	ds_read_b128 v[8:11], v249 offset:32768
	ds_read_b128 v[192:195], v172 offset:40960
	ds_read_b128 v[196:199], v249 offset:40960
	ds_read_b128 v[12:15], v173 offset:32768
	ds_read_b128 v[200:203], v253 offset:32768
	ds_read_b128 v[204:207], v173 offset:40960
	ds_read_b128 v[208:211], v253 offset:40960
	s_waitcnt lgkmcnt(7)
	v_mfma_f32_32x32x16_f16 v[82:97], v[4:7], v[114:117], 0
	ds_read_b128 v[4:7], v174 offset:32768
	ds_read_b128 v[212:215], v254 offset:32768
	ds_read_b128 v[216:219], v174 offset:40960
	ds_read_b128 v[220:223], v254 offset:40960
	ds_read_b128 v[224:227], v175 offset:32768
	ds_read_b128 v[228:231], v255 offset:32768
	ds_read_b128 v[232:235], v175 offset:40960
	ds_read_b128 v[236:239], v255 offset:40960
	v_add_f32_e32 v3, 0, v190
	v_add_f32_e32 v3, v191, v3
	v_add_f32_e32 v3, v188, v3
	v_add_f32_e32 v3, v189, v3
	v_add_f32_e32 v3, v186, v3
	v_add_f32_e32 v3, v187, v3
	s_waitcnt lgkmcnt(11)
	v_mfma_f32_32x32x16_f16 v[82:97], v[12:15], v[118:121], v[82:97]
	v_add_f32_e32 v3, v184, v3
	v_add_f32_e32 v3, v185, v3
	v_add_f32_e32 v3, v182, v3
	v_add_f32_e32 v3, v183, v3
	v_add_f32_e32 v3, v156, v3
	v_add_f32_e32 v3, v157, v3
	v_exp_f32_e32 v12, v98
	s_waitcnt lgkmcnt(7)
	v_mfma_f32_32x32x16_f16 v[82:97], v[4:7], v[122:125], v[82:97]
	v_add_f32_e32 v3, v148, v3
	v_exp_f32_e32 v13, v99
	v_add_f32_e32 v3, v149, v3
	v_exp_f32_e32 v14, v100
	v_add_f32_e32 v3, v146, v3
	v_exp_f32_e32 v15, v101
	v_add_f32_e32 v3, v147, v3
	s_waitcnt lgkmcnt(3)
	v_mfma_f32_32x32x16_f16 v[82:97], v[224:227], v[126:129], v[82:97]
	v_exp_f32_e32 v16, v102
	v_add_f32_e32 v3, v12, v3
	v_exp_f32_e32 v17, v103
	v_add_f32_e32 v3, v13, v3
	v_exp_f32_e32 v98, v104
	v_add_f32_e32 v3, v14, v3
	v_exp_f32_e32 v99, v105
	v_mfma_f32_32x32x16_f16 v[82:97], v[8:11], v[130:133], v[82:97]
	v_add_f32_e32 v3, v15, v3
	v_exp_f32_e32 v100, v106
	v_add_f32_e32 v3, v16, v3
	v_exp_f32_e32 v101, v107
	v_add_f32_e32 v3, v17, v3
	v_exp_f32_e32 v102, v108
	v_add_f32_e32 v3, v98, v3
	v_mfma_f32_32x32x16_f16 v[82:97], v[200:203], v[134:137], v[82:97]
	v_exp_f32_e32 v103, v109
	v_add_f32_e32 v3, v99, v3
	v_exp_f32_e32 v104, v110
	v_add_f32_e32 v3, v100, v3
	v_exp_f32_e32 v105, v111
	v_add_f32_e32 v3, v101, v3
	v_exp_f32_e32 v106, v112
	v_mfma_f32_32x32x16_f16 v[82:97], v[212:215], v[138:141], v[82:97]
	v_add_f32_e32 v3, v102, v3
	v_exp_f32_e32 v107, v113
	v_add_f32_e32 v3, v103, v3
	v_add_f32_e32 v3, v104, v3
	v_add_f32_e32 v3, v105, v3
	v_add_f32_e32 v3, v106, v3
	v_add_f32_e32 v3, v107, v3
	s_waitcnt lgkmcnt(2)
	v_mfma_f32_32x32x16_f16 v[82:97], v[228:231], v[142:145], v[82:97]
	v_mov_b32_e32 v180, v3
	v_cvt_pk_f16_f32 v4, v190, v191
	v_cvt_pk_f16_f32 v5, v188, v189
	v_cvt_pk_f16_f32 v6, v186, v187
	v_cvt_pk_f16_f32 v7, v184, v185
	v_cvt_pk_f16_f32 v8, v182, v183
	v_cvt_pk_f16_f32 v9, v156, v157
	v_cvt_pk_f16_f32 v10, v148, v149
	v_cvt_pk_f16_f32 v11, v146, v147
	v_cvt_pk_f16_f32 v12, v12, v13
	v_cvt_pk_f16_f32 v13, v14, v15
	v_cvt_pk_f16_f32 v14, v16, v17
	v_cvt_pk_f16_f32 v15, v98, v99
	v_cvt_pk_f16_f32 v146, v100, v101
	v_cvt_pk_f16_f32 v147, v102, v103
	v_cvt_pk_f16_f32 v148, v104, v105
	v_cvt_pk_f16_f32 v149, v106, v107
	s_nop 1
	v_permlane32_swap_b32_e32 v3, v180
	v_permlane32_swap_b32_e32 v4, v6
	v_permlane32_swap_b32_e32 v5, v7
	v_permlane32_swap_b32_e32 v8, v10
	v_permlane32_swap_b32_e32 v9, v11
	v_permlane32_swap_b32_e32 v12, v14
	v_permlane32_swap_b32_e32 v13, v15
	v_permlane32_swap_b32_e32 v146, v148
	v_permlane32_swap_b32_e32 v147, v149
	s_add_u32 s4, s74, 0x10000
	s_addc_u32 s5, s75, 0
	s_add_u32 s6, s76, 0x8000
	s_addc_u32 s7, s77, 0
	s_add_i32 m0, s69, 0x10000
	v_mfma_f32_32x32x16_f16 v[98:113], v[192:195], v[114:117], 0
	global_load_lds_dwordx4 v154, s[4:5]
	s_add_i32 m0, s69, 0x12000
	v_mfma_f32_32x32x16_f16 v[98:113], v[204:207], v[118:121], v[98:113]
	global_load_lds_dwordx4 v250, s[4:5]
	s_add_i32 m0, s69, 0x14000
	v_mfma_f32_32x32x16_f16 v[98:113], v[216:219], v[122:125], v[98:113]
	global_load_lds_dwordx4 v251, s[4:5]
	s_add_i32 m0, s69, 0x16000
	s_waitcnt lgkmcnt(0)
	v_mfma_f32_32x32x16_f16 v[98:113], v[232:235], v[126:129], v[98:113]
	global_load_lds_dwordx4 v252, s[4:5]
	s_add_i32 m0, s69, 0x8000
	v_mfma_f32_32x32x16_f16 v[98:113], v[196:199], v[130:133], v[98:113]
	global_load_lds_dwordx4 v154, s[6:7]
	s_add_i32 m0, s69, 0xa000
	v_mfma_f32_32x32x16_f16 v[98:113], v[208:211], v[134:137], v[98:113]
	global_load_lds_dwordx4 v250, s[6:7]
	s_add_i32 m0, s69, 0xc000
	v_mfma_f32_32x32x16_f16 v[98:113], v[220:223], v[138:141], v[98:113]
	global_load_lds_dwordx4 v251, s[6:7]
	s_add_i32 m0, s69, 0xe000
	v_mfma_f32_32x32x16_f16 v[98:113], v[236:239], v[142:145], v[98:113]
	global_load_lds_dwordx4 v252, s[6:7]
	s_add_i32 s4, s68, 0xffffff80
	s_cmp_le_i32 s4, s93
	v_add_u32_e32 v181, 0x80, v179
	s_cbranch_scc1 .LBB1_14
	v_cmp_gt_i32_e64 s[62:63], 26, v181
	v_cmp_gt_i32_e64 s[64:65], 27, v181
	v_cmp_gt_i32_e64 s[60:61], 25, v181
	s_and_b64 s[62:63], s[64:65], s[62:63]
	v_cmp_gt_i32_e64 s[58:59], 24, v181
	s_and_b64 s[60:61], s[62:63], s[60:61]
	v_cmp_gt_i32_e64 s[56:57], 19, v181
	s_and_b64 s[58:59], s[60:61], s[58:59]
	v_cmp_gt_i32_e64 s[54:55], 18, v181
	s_and_b64 s[56:57], s[58:59], s[56:57]
	v_cmp_gt_i32_e64 s[52:53], 17, v181
	s_and_b64 s[54:55], s[56:57], s[54:55]
	v_cmp_gt_i32_e64 s[50:51], 16, v181
	s_and_b64 s[52:53], s[54:55], s[52:53]
	v_cmp_gt_i32_e64 s[48:49], 11, v181
	s_and_b64 s[50:51], s[52:53], s[50:51]
	v_cmp_gt_i32_e64 s[46:47], 10, v181
	s_and_b64 s[48:49], s[50:51], s[48:49]
	v_cmp_gt_i32_e64 s[44:45], 9, v181
	s_and_b64 s[46:47], s[48:49], s[46:47]
	v_cmp_gt_i32_e64 s[42:43], 8, v181
	s_and_b64 s[44:45], s[46:47], s[44:45]
	v_cmp_gt_i32_e64 s[40:41], 3, v181
	s_and_b64 s[42:43], s[44:45], s[42:43]
	v_cmp_gt_i32_e64 s[38:39], 2, v181
	s_and_b64 s[40:41], s[42:43], s[40:41]
	v_cmp_gt_i32_e64 s[36:37], 1, v181
	s_and_b64 s[38:39], s[40:41], s[38:39]
	v_cmp_gt_i32_e64 s[34:35], 0, v181
	s_and_b64 s[36:37], s[38:39], s[36:37]
	s_and_b64 s[34:35], s[36:37], s[34:35]
	v_cmp_gt_i32_e64 s[30:31], 58, v181
	v_cndmask_b32_e64 v82, v82, v164, s[34:35]
	v_cmp_gt_i32_e64 s[34:35], 59, v181
	v_cmp_gt_i32_e64 s[28:29], 57, v181
	s_and_b64 s[30:31], s[34:35], s[30:31]
	v_cmp_gt_i32_e64 s[26:27], 56, v181
	s_and_b64 s[28:29], s[30:31], s[28:29]
	v_cmp_gt_i32_e64 s[24:25], 51, v181
	s_and_b64 s[26:27], s[28:29], s[26:27]
	v_cmp_gt_i32_e64 s[22:23], 50, v181
	s_and_b64 s[24:25], s[26:27], s[24:25]
	v_cmp_gt_i32_e64 s[20:21], 49, v181
	s_and_b64 s[22:23], s[24:25], s[22:23]
	v_cmp_gt_i32_e64 s[18:19], 48, v181
	s_and_b64 s[20:21], s[22:23], s[20:21]
	v_cmp_gt_i32_e64 s[16:17], 43, v181
	s_and_b64 s[18:19], s[20:21], s[18:19]
	v_cmp_gt_i32_e64 s[14:15], 42, v181
	s_and_b64 s[16:17], s[18:19], s[16:17]
	v_cmp_gt_i32_e64 s[12:13], 41, v181
	s_and_b64 s[14:15], s[16:17], s[14:15]
	v_cmp_gt_i32_e64 s[10:11], 40, v181
	s_and_b64 s[12:13], s[14:15], s[12:13]
	v_cmp_gt_i32_e64 s[8:9], 35, v181
	s_and_b64 s[10:11], s[12:13], s[10:11]
	v_cmp_gt_i32_e64 s[6:7], 34, v181
	s_and_b64 s[8:9], s[10:11], s[8:9]
	v_cmp_gt_i32_e64 s[4:5], 33, v181
	s_and_b64 s[6:7], s[8:9], s[6:7]
	v_cmp_gt_i32_e32 vcc, 32, v181
	s_and_b64 s[4:5], s[6:7], s[4:5]
	s_and_b64 vcc, s[4:5], vcc
	v_cndmask_b32_e64 v97, v97, v164, s[64:65]
	v_cndmask_b32_e64 v96, v96, v164, s[62:63]
	v_cndmask_b32_e64 v95, v95, v164, s[60:61]
	v_cndmask_b32_e64 v94, v94, v164, s[58:59]
	v_cndmask_b32_e64 v93, v93, v164, s[56:57]
	v_cndmask_b32_e64 v92, v92, v164, s[54:55]
	v_cndmask_b32_e64 v91, v91, v164, s[52:53]
	v_cndmask_b32_e64 v90, v90, v164, s[50:51]
	v_cndmask_b32_e64 v89, v89, v164, s[48:49]
	v_cndmask_b32_e64 v88, v88, v164, s[46:47]
	v_cndmask_b32_e64 v87, v87, v164, s[44:45]
	v_cndmask_b32_e64 v86, v86, v164, s[42:43]
	v_cndmask_b32_e64 v85, v85, v164, s[40:41]
	v_cndmask_b32_e64 v84, v84, v164, s[38:39]
	v_cndmask_b32_e64 v83, v83, v164, s[36:37]
	v_cndmask_b32_e64 v113, v113, v164, s[34:35]
	v_cndmask_b32_e64 v112, v112, v164, s[30:31]
	v_cndmask_b32_e64 v111, v111, v164, s[28:29]
	v_cndmask_b32_e64 v110, v110, v164, s[26:27]
	v_cndmask_b32_e64 v109, v109, v164, s[24:25]
	v_cndmask_b32_e64 v108, v108, v164, s[22:23]
	v_cndmask_b32_e64 v107, v107, v164, s[20:21]
	v_cndmask_b32_e64 v106, v106, v164, s[18:19]
	v_cndmask_b32_e64 v105, v105, v164, s[16:17]
	v_cndmask_b32_e64 v104, v104, v164, s[14:15]
	v_cndmask_b32_e64 v103, v103, v164, s[12:13]
	v_cndmask_b32_e64 v102, v102, v164, s[10:11]
	v_cndmask_b32_e64 v101, v101, v164, s[8:9]
	v_cndmask_b32_e64 v100, v100, v164, s[6:7]
	v_cndmask_b32_e64 v99, v99, v164, s[4:5]
	v_cndmask_b32_e32 v98, v98, v164, vcc

.Lnoresc1:
	s_waitcnt vmcnt(0)
	s_barrier
	ds_read_b128 v[4:7], v172
	ds_read_b128 v[8:11], v249
	v_exp_f32_e32 v183, v183
	v_exp_f32_e32 v246, v192
	v_exp_f32_e32 v247, v193
	s_waitcnt lgkmcnt(1)
	v_mfma_f32_32x32x16_f16 v[98:113], v[4:7], v[114:117], 0
	ds_read_b128 v[4:7], v172 offset:8192
	ds_read_b128 v[12:15], v249 offset:8192
	v_exp_f32_e32 v218, v218
	v_exp_f32_e32 v219, v219
	v_exp_f32_e32 v220, v220
	v_exp_f32_e32 v221, v221
	v_exp_f32_e32 v222, v222
	v_exp_f32_e32 v223, v223
	s_waitcnt lgkmcnt(1)
	v_mfma_f32_32x32x16_f16 v[82:97], v[4:7], v[114:117], 0
	ds_read_b128 v[4:7], v173
	ds_read_b128 v[146:149], v173 offset:8192
	ds_read_b128 v[184:187], v253
	v_exp_f32_e32 v224, v224
	v_exp_f32_e32 v225, v225
	v_exp_f32_e32 v226, v226
	v_exp_f32_e32 v178, v178
	s_waitcnt lgkmcnt(2)
	v_mfma_f32_32x32x16_f16 v[98:113], v[4:7], v[118:121], v[98:113]
	ds_read_b128 v[188:191], v253 offset:8192
	ds_read_b128 v[4:7], v174
	ds_read_b128 v[194:197], v254
	ds_read_b128 v[198:201], v174 offset:8192
	ds_read_b128 v[202:205], v254 offset:8192
	ds_read_b128 v[206:209], v175
	ds_read_b128 v[210:213], v255
	s_waitcnt lgkmcnt(8)
	v_mfma_f32_32x32x16_f16 v[82:97], v[146:149], v[118:121], v[82:97]
	ds_read_b128 v[146:149], v175 offset:8192
	ds_read_b128 v[214:217], v255 offset:8192
	s_waitcnt lgkmcnt(7)
	v_mfma_f32_32x32x16_f16 v[98:113], v[4:7], v[122:125], v[98:113]
	v_add_f32_e32 v4, 0, v230
	v_add_f32_e32 v4, v231, v4
	v_add_f32_e32 v4, v232, v4
	v_add_f32_e32 v4, v233, v4
	v_add_f32_e32 v4, v234, v4
	v_add_f32_e32 v4, v235, v4
	v_add_f32_e32 v4, v236, v4
	s_waitcnt lgkmcnt(5)
	v_mfma_f32_32x32x16_f16 v[82:97], v[198:201], v[122:125], v[82:97]
	v_add_f32_e32 v4, v237, v4
	v_add_f32_e32 v4, v238, v4
	v_add_f32_e32 v4, v239, v4
	v_add_f32_e32 v4, v240, v4
	v_add_f32_e32 v4, v241, v4
	v_add_f32_e32 v4, v242, v4
	v_add_f32_e32 v4, v243, v4
	s_waitcnt lgkmcnt(3)
	v_mfma_f32_32x32x16_f16 v[98:113], v[206:209], v[126:129], v[98:113]
	v_add_f32_e32 v4, v244, v4
	v_add_f32_e32 v4, v245, v4
	v_add_f32_e32 v4, v183, v4
	v_add_f32_e32 v4, v246, v4
	v_add_f32_e32 v4, v247, v4
	v_add_f32_e32 v4, v218, v4
	v_add_f32_e32 v4, v219, v4
	s_waitcnt lgkmcnt(1)
	v_mfma_f32_32x32x16_f16 v[82:97], v[146:149], v[126:129], v[82:97]
	v_add_f32_e32 v4, v220, v4
	v_add_f32_e32 v4, v221, v4
	v_add_f32_e32 v4, v222, v4
	v_exp_f32_e32 v198, v227
	v_add_f32_e32 v4, v223, v4
	v_exp_f32_e32 v199, v228
	v_add_f32_e32 v4, v224, v4
	v_mfma_f32_32x32x16_f16 v[98:113], v[8:11], v[130:133], v[98:113]
	v_exp_f32_e32 v200, v229
	v_add_f32_e32 v4, v225, v4
	v_add_f32_e32 v4, v226, v4
	v_add_f32_e32 v4, v198, v4
	v_add_f32_e32 v4, v199, v4
	v_add_f32_e32 v4, v200, v4
	v_add_f32_e32 v192, v178, v4
	v_mfma_f32_32x32x16_f16 v[82:97], v[12:15], v[130:133], v[82:97]
	v_mov_b32_e32 v193, v192
	v_cvt_pk_f16_f32 v4, v230, v231
	v_cvt_pk_f16_f32 v5, v232, v233
	v_cvt_pk_f16_f32 v6, v234, v235
	v_cvt_pk_f16_f32 v7, v236, v237
	v_cvt_pk_f16_f32 v8, v238, v239
	v_cvt_pk_f16_f32 v9, v240, v241
	v_mfma_f32_32x32x16_f16 v[98:113], v[184:187], v[134:137], v[98:113]
	v_cvt_pk_f16_f32 v10, v242, v243
	v_cvt_pk_f16_f32 v11, v244, v245
	v_cvt_pk_f16_f32 v12, v183, v246
	v_cvt_pk_f16_f32 v13, v247, v218
	v_cvt_pk_f16_f32 v14, v219, v220
	v_cvt_pk_f16_f32 v15, v221, v222
	v_cvt_pk_f16_f32 v146, v223, v224
	v_mfma_f32_32x32x16_f16 v[82:97], v[188:191], v[134:137], v[82:97]
	v_cvt_pk_f16_f32 v147, v225, v226
	v_cvt_pk_f16_f32 v148, v198, v199
	v_cvt_pk_f16_f32 v149, v200, v178
	v_permlane32_swap_b32_e32 v192, v193
	v_permlane32_swap_b32_e32 v4, v6
	v_mfma_f32_32x32x16_f16 v[98:113], v[194:197], v[138:141], v[98:113]
	v_permlane32_swap_b32_e32 v5, v7
	v_permlane32_swap_b32_e32 v8, v10
	v_permlane32_swap_b32_e32 v9, v11
	v_permlane32_swap_b32_e32 v12, v14
	v_mfma_f32_32x32x16_f16 v[82:97], v[202:205], v[138:141], v[82:97]
	v_permlane32_swap_b32_e32 v13, v15
	v_permlane32_swap_b32_e32 v146, v148
	v_permlane32_swap_b32_e32 v147, v149
	v_mfma_f32_32x32x16_f16 v[98:113], v[210:213], v[142:145], v[98:113]
	s_waitcnt lgkmcnt(0)
	v_mfma_f32_32x32x16_f16 v[82:97], v[214:217], v[142:145], v[82:97]
	s_add_i32 s72, s72, 2
	s_cmp_gt_u32 s72, s83
	s_cbranch_scc1 .LBB1_20
	s_add_u32 s4, s74, 0x18000
	s_addc_u32 s5, s75, 0
	s_add_i32 m0, s69, 0x18000
	s_nop 0
	global_load_lds_dwordx4 v154, s[4:5]
	s_add_i32 m0, s69, 0x1a000
	s_nop 0
	global_load_lds_dwordx4 v250, s[4:5]
	s_add_i32 m0, s69, 0x1c000
	s_nop 0
	global_load_lds_dwordx4 v251, s[4:5]
	s_add_i32 m0, s69, 0x1e000
	s_nop 0
	global_load_lds_dwordx4 v252, s[4:5]

.LBB1_28:
	ds_read_b128 v[4:7], v172 offset:32768
	ds_read_b128 v[8:11], v249 offset:32768
	ds_read_b128 v[192:195], v172 offset:40960
	ds_read_b128 v[196:199], v249 offset:40960
	ds_read_b128 v[12:15], v173 offset:32768
	ds_read_b128 v[200:203], v253 offset:32768
	ds_read_b128 v[204:207], v173 offset:40960
	ds_read_b128 v[208:211], v253 offset:40960
	s_waitcnt lgkmcnt(7)
	v_mfma_f32_32x32x16_f16 v[82:97], v[4:7], v[114:117], 0
	ds_read_b128 v[4:7], v174 offset:32768
	ds_read_b128 v[212:215], v254 offset:32768
	ds_read_b128 v[216:219], v174 offset:40960
	ds_read_b128 v[220:223], v254 offset:40960
	ds_read_b128 v[224:227], v175 offset:32768
	ds_read_b128 v[228:231], v255 offset:32768
	ds_read_b128 v[232:235], v175 offset:40960
	ds_read_b128 v[172:175], v255 offset:40960
	v_exp_f32_e32 v3, v98
	v_exp_f32_e32 v98, v103
	v_exp_f32_e32 v103, v108
	v_exp_f32_e32 v108, v113
	s_waitcnt lgkmcnt(11)
	v_mfma_f32_32x32x16_f16 v[82:97], v[12:15], v[118:121], v[82:97]
	v_exp_f32_e32 v12, v99
	v_exp_f32_e32 v13, v100
	v_exp_f32_e32 v14, v101
	v_exp_f32_e32 v15, v102
	v_exp_f32_e32 v99, v104
	v_exp_f32_e32 v100, v105
	v_exp_f32_e32 v101, v106
	s_waitcnt lgkmcnt(7)
	v_mfma_f32_32x32x16_f16 v[82:97], v[4:7], v[122:125], v[82:97]
	v_add_f32_e32 v4, 0, v190
	v_add_f32_e32 v4, v191, v4
	v_add_f32_e32 v4, v188, v4
	v_add_f32_e32 v4, v189, v4
	v_add_f32_e32 v4, v186, v4
	v_add_f32_e32 v4, v187, v4
	v_add_f32_e32 v4, v184, v4
	s_waitcnt lgkmcnt(3)
	v_mfma_f32_32x32x16_f16 v[82:97], v[224:227], v[126:129], v[82:97]
	v_add_f32_e32 v4, v185, v4
	v_add_f32_e32 v4, v182, v4
	v_add_f32_e32 v4, v183, v4
	v_add_f32_e32 v4, v156, v4
	v_add_f32_e32 v4, v157, v4
	v_add_f32_e32 v4, v148, v4
	v_add_f32_e32 v4, v149, v4
	v_mfma_f32_32x32x16_f16 v[82:97], v[8:11], v[130:133], v[82:97]
	v_add_f32_e32 v4, v146, v4
	v_add_f32_e32 v4, v147, v4
	v_add_f32_e32 v4, v3, v4
	v_add_f32_e32 v4, v12, v4
	v_add_f32_e32 v4, v13, v4
	v_add_f32_e32 v4, v14, v4
	v_add_f32_e32 v4, v15, v4
	v_mfma_f32_32x32x16_f16 v[82:97], v[200:203], v[134:137], v[82:97]
	v_exp_f32_e32 v102, v107
	v_add_f32_e32 v4, v98, v4
	v_add_f32_e32 v4, v99, v4
	v_exp_f32_e32 v104, v109
	v_add_f32_e32 v4, v100, v4
	v_exp_f32_e32 v105, v110
	v_add_f32_e32 v4, v101, v4
	v_mfma_f32_32x32x16_f16 v[82:97], v[212:215], v[138:141], v[82:97]
	v_exp_f32_e32 v106, v111
	v_add_f32_e32 v4, v102, v4
	v_exp_f32_e32 v107, v112
	v_add_f32_e32 v4, v103, v4
	v_add_f32_e32 v4, v104, v4
	v_add_f32_e32 v4, v105, v4
	v_add_f32_e32 v4, v106, v4
	s_waitcnt lgkmcnt(2)
	v_mfma_f32_32x32x16_f16 v[82:97], v[228:231], v[142:145], v[82:97]
	v_add_f32_e32 v4, v107, v4
	v_add_f32_e32 v16, v108, v4
	v_mov_b32_e32 v17, v16
	v_cvt_pk_f16_f32 v4, v190, v191
	v_cvt_pk_f16_f32 v5, v188, v189
	v_cvt_pk_f16_f32 v6, v186, v187
	v_cvt_pk_f16_f32 v7, v184, v185
	v_cvt_pk_f16_f32 v8, v182, v183
	v_cvt_pk_f16_f32 v9, v156, v157
	v_cvt_pk_f16_f32 v10, v148, v149
	v_cvt_pk_f16_f32 v11, v146, v147
	v_cvt_pk_f16_f32 v12, v3, v12
	v_cvt_pk_f16_f32 v13, v13, v14
	v_cvt_pk_f16_f32 v14, v15, v98
	v_cvt_pk_f16_f32 v15, v99, v100
	v_cvt_pk_f16_f32 v146, v101, v102
	v_cvt_pk_f16_f32 v147, v103, v104
	v_cvt_pk_f16_f32 v148, v105, v106
	v_cvt_pk_f16_f32 v149, v107, v108
	s_nop 1
	v_permlane32_swap_b32_e32 v16, v17
	v_permlane32_swap_b32_e32 v4, v6
	v_permlane32_swap_b32_e32 v5, v7
	v_permlane32_swap_b32_e32 v8, v10
	v_permlane32_swap_b32_e32 v9, v11
	v_permlane32_swap_b32_e32 v12, v14
	v_permlane32_swap_b32_e32 v13, v15
	v_permlane32_swap_b32_e32 v146, v148
	v_permlane32_swap_b32_e32 v147, v149
	s_lshl_b64 s[2:3], s[72:73], 15
	s_add_u32 s2, s76, s2
	s_addc_u32 s3, s77, s3
	v_lshl_add_u64 v[154:155], v[152:153], 1, s[2:3]
	s_lshl_b32 s2, s33, 10
	s_add_i32 s2, s2, 0
	s_add_i32 m0, s2, 0x8000
	s_mov_b64 s[4:5], 0x2000
	global_load_lds_dwordx4 v[154:155], off
	v_lshl_add_u64 v[156:157], v[154:155], 0, s[4:5]
	s_add_i32 m0, s2, 0xa000
	s_mov_b64 s[4:5], 0x4000
	global_load_lds_dwordx4 v[156:157], off
	v_lshl_add_u64 v[156:157], v[154:155], 0, s[4:5]
	s_add_i32 m0, s2, 0xc000
	s_mov_b64 s[4:5], 0x6000
	global_load_lds_dwordx4 v[156:157], off
	v_lshl_add_u64 v[154:155], v[154:155], 0, s[4:5]
	s_add_i32 m0, s2, 0xe000
	v_mfma_f32_32x32x16_f16 v[98:113], v[192:195], v[114:117], 0
	global_load_lds_dwordx4 v[154:155], off
	v_mfma_f32_32x32x16_f16 v[98:113], v[204:207], v[118:121], v[98:113]
	v_mfma_f32_32x32x16_f16 v[98:113], v[216:219], v[122:125], v[98:113]
	s_waitcnt lgkmcnt(0)
	v_mfma_f32_32x32x16_f16 v[98:113], v[232:235], v[126:129], v[98:113]
	v_mfma_f32_32x32x16_f16 v[98:113], v[196:199], v[130:133], v[98:113]
	v_mfma_f32_32x32x16_f16 v[98:113], v[208:211], v[134:137], v[98:113]
	v_mfma_f32_32x32x16_f16 v[98:113], v[220:223], v[138:141], v[98:113]
	v_mfma_f32_32x32x16_f16 v[98:113], v[172:175], v[142:145], v[98:113]
	s_lshl_b32 s2, s72, 7
	s_add_i32 s2, s2, s82
	s_or_b32 s3, s2, 63
	s_cmp_le_i32 s3, s93
	v_subrev_u32_e32 v3, s2, v171
	s_cbranch_scc1 .LBB1_30
	v_cmp_gt_i32_e64 s[60:61], 26, v3
	v_cmp_gt_i32_e64 s[62:63], 27, v3
	v_cmp_gt_i32_e64 s[58:59], 25, v3
	s_and_b64 s[60:61], s[62:63], s[60:61]
	v_cmp_gt_i32_e64 s[56:57], 24, v3
	s_and_b64 s[58:59], s[60:61], s[58:59]
	v_cmp_gt_i32_e64 s[54:55], 19, v3
	s_and_b64 s[56:57], s[58:59], s[56:57]
	v_cmp_gt_i32_e64 s[52:53], 18, v3
	s_and_b64 s[54:55], s[56:57], s[54:55]
	v_cmp_gt_i32_e64 s[50:51], 17, v3
	s_and_b64 s[52:53], s[54:55], s[52:53]
	v_cmp_gt_i32_e64 s[48:49], 16, v3
	s_and_b64 s[50:51], s[52:53], s[50:51]
	v_cmp_gt_i32_e64 s[46:47], 11, v3
	s_and_b64 s[48:49], s[50:51], s[48:49]
	v_cmp_gt_i32_e64 s[44:45], 10, v3
	s_and_b64 s[46:47], s[48:49], s[46:47]
	v_cmp_gt_i32_e64 s[42:43], 9, v3
	s_and_b64 s[44:45], s[46:47], s[44:45]
	v_cmp_gt_i32_e64 s[40:41], 8, v3
	s_and_b64 s[42:43], s[44:45], s[42:43]
	v_cmp_gt_i32_e64 s[38:39], 3, v3
	s_and_b64 s[40:41], s[42:43], s[40:41]
	v_cmp_gt_i32_e64 s[36:37], 2, v3
	s_and_b64 s[38:39], s[40:41], s[38:39]
	v_cmp_gt_i32_e64 s[34:35], 1, v3
	s_and_b64 s[36:37], s[38:39], s[36:37]
	v_cmp_gt_i32_e64 s[30:31], 0, v3
	s_and_b64 s[34:35], s[36:37], s[34:35]
	s_and_b64 s[30:31], s[34:35], s[30:31]
	v_cmp_gt_i32_e64 s[28:29], 58, v3
	v_cndmask_b32_e64 v82, v82, v164, s[30:31]
	v_cmp_gt_i32_e64 s[30:31], 59, v3
	v_cmp_gt_i32_e64 s[26:27], 57, v3
	s_and_b64 s[28:29], s[30:31], s[28:29]
	v_cmp_gt_i32_e64 s[24:25], 56, v3
	s_and_b64 s[26:27], s[28:29], s[26:27]
	v_cmp_gt_i32_e64 s[22:23], 51, v3
	s_and_b64 s[24:25], s[26:27], s[24:25]
	v_cmp_gt_i32_e64 s[20:21], 50, v3
	s_and_b64 s[22:23], s[24:25], s[22:23]
	v_cmp_gt_i32_e64 s[18:19], 49, v3
	s_and_b64 s[20:21], s[22:23], s[20:21]
	v_cmp_gt_i32_e64 s[16:17], 48, v3
	s_and_b64 s[18:19], s[20:21], s[18:19]
	v_cmp_gt_i32_e64 s[14:15], 43, v3
	s_and_b64 s[16:17], s[18:19], s[16:17]
	v_cmp_gt_i32_e64 s[12:13], 42, v3
	s_and_b64 s[14:15], s[16:17], s[14:15]
	v_cmp_gt_i32_e64 s[10:11], 41, v3
	s_and_b64 s[12:13], s[14:15], s[12:13]
	v_cmp_gt_i32_e64 s[8:9], 40, v3
	s_and_b64 s[10:11], s[12:13], s[10:11]
	v_cmp_gt_i32_e64 s[6:7], 35, v3
	s_and_b64 s[8:9], s[10:11], s[8:9]
	v_cmp_gt_i32_e64 s[4:5], 34, v3
	s_and_b64 s[6:7], s[8:9], s[6:7]
	v_cmp_gt_i32_e64 s[2:3], 33, v3
	s_and_b64 s[4:5], s[6:7], s[4:5]
	v_cmp_gt_i32_e32 vcc, 32, v3
	s_and_b64 s[2:3], s[4:5], s[2:3]
	s_and_b64 vcc, s[2:3], vcc
	v_cndmask_b32_e64 v97, v97, v164, s[62:63]
	v_cndmask_b32_e64 v96, v96, v164, s[60:61]
	v_cndmask_b32_e64 v95, v95, v164, s[58:59]
	v_cndmask_b32_e64 v94, v94, v164, s[56:57]
	v_cndmask_b32_e64 v93, v93, v164, s[54:55]
	v_cndmask_b32_e64 v92, v92, v164, s[52:53]
	v_cndmask_b32_e64 v91, v91, v164, s[50:51]
	v_cndmask_b32_e64 v90, v90, v164, s[48:49]
	v_cndmask_b32_e64 v89, v89, v164, s[46:47]
	v_cndmask_b32_e64 v88, v88, v164, s[44:45]
	v_cndmask_b32_e64 v87, v87, v164, s[42:43]
	v_cndmask_b32_e64 v86, v86, v164, s[40:41]
	v_cndmask_b32_e64 v85, v85, v164, s[38:39]
	v_cndmask_b32_e64 v84, v84, v164, s[36:37]
	v_cndmask_b32_e64 v83, v83, v164, s[34:35]
	v_cndmask_b32_e64 v113, v113, v164, s[30:31]
	v_cndmask_b32_e64 v112, v112, v164, s[28:29]
	v_cndmask_b32_e64 v111, v111, v164, s[26:27]
	v_cndmask_b32_e64 v110, v110, v164, s[24:25]
	v_cndmask_b32_e64 v109, v109, v164, s[22:23]
	v_cndmask_b32_e64 v108, v108, v164, s[20:21]
	v_cndmask_b32_e64 v107, v107, v164, s[18:19]
	v_cndmask_b32_e64 v106, v106, v164, s[16:17]
	v_cndmask_b32_e64 v105, v105, v164, s[14:15]
	v_cndmask_b32_e64 v104, v104, v164, s[12:13]
	v_cndmask_b32_e64 v103, v103, v164, s[10:11]
	v_cndmask_b32_e64 v102, v102, v164, s[8:9]
	v_cndmask_b32_e64 v101, v101, v164, s[6:7]
	v_cndmask_b32_e64 v100, v100, v164, s[4:5]
	v_cndmask_b32_e64 v99, v99, v164, s[2:3]
	v_cndmask_b32_e32 v98, v98, v164, vcc

	.amdhsa_kernel _Z11attn_kernelPKDF16_S0_S0_PDF16_PKfS1_
		.amdhsa_group_segment_fixed_size 0
		.amdhsa_private_segment_fixed_size 0
		.amdhsa_kernarg_size 48
		.amdhsa_user_sgpr_count 2
		.amdhsa_user_sgpr_dispatch_ptr 0
		.amdhsa_user_sgpr_queue_ptr 0
		.amdhsa_user_sgpr_kernarg_segment_ptr 1
		.amdhsa_user_sgpr_dispatch_id 0
		.amdhsa_user_sgpr_kernarg_preload_length 0
		.amdhsa_user_sgpr_kernarg_preload_offset 0
		.amdhsa_user_sgpr_private_segment_size 0
		.amdhsa_uses_dynamic_stack 0
		.amdhsa_enable_private_segment 0
		.amdhsa_system_sgpr_workgroup_id_x 1
		.amdhsa_system_sgpr_workgroup_id_y 0
		.amdhsa_system_sgpr_workgroup_id_z 0
		.amdhsa_system_sgpr_workgroup_info 0
		.amdhsa_system_vgpr_workitem_id 0
		.amdhsa_next_free_vgpr 256
		.amdhsa_next_free_sgpr 100
		.amdhsa_accum_offset 256
		.amdhsa_reserve_vcc 1
		.amdhsa_float_round_mode_32 0
		.amdhsa_float_round_mode_16_64 0
		.amdhsa_float_denorm_mode_32 3
		.amdhsa_float_denorm_mode_16_64 3
		.amdhsa_dx10_clamp 1
		.amdhsa_ieee_mode 1
		.amdhsa_fp16_overflow 0
		.amdhsa_tg_split 0
		.amdhsa_exception_fp_ieee_invalid_op 0
		.amdhsa_exception_fp_denorm_src 0
		.amdhsa_exception_fp_ieee_div_zero 0
		.amdhsa_exception_fp_ieee_overflow 0
		.amdhsa_exception_fp_ieee_underflow 0
		.amdhsa_exception_fp_ieee_inexact 0
		.amdhsa_exception_int_div_zero 0
	.end_amdhsa_kernel

.LBB2_33:
	global_load_dwordx4 v[34:37], v134, s[18:19]
	global_load_dwordx4 v[38:41], v134, s[18:19] offset:256
	v_add_u32_e32 v62, 0x11000, v131
	v_add_u32_e32 v63, 0x11080, v131
	v_add_u32_e32 v64, 0x12100, v131
	v_add_u32_e32 v65, 0x12180, v131
	v_add_u32_e32 v66, 0x13200, v131
	v_add_u32_e32 v67, 0x13280, v131
	s_mov_b64 vcc, s[0:1]
	s_waitcnt vmcnt(1)
	v_pk_add_f32 v[30:31], v[30:31], v[34:35]
	s_waitcnt vmcnt(0)
	v_pk_add_f32 v[26:27], v[26:27], v[38:39]
	v_pk_add_f32 v[28:29], v[28:29], v[40:41]
	v_pk_add_f32 v[10:11], v[10:11], v[38:39]
	v_pk_add_f32 v[12:13], v[12:13], v[40:41]
	v_pk_add_f32 v[32:33], v[32:33], v[36:37]
	v_pk_add_f32 v[22:23], v[22:23], v[34:35]
	v_pk_add_f32 v[24:25], v[24:25], v[36:37]
	v_pk_add_f32 v[18:19], v[18:19], v[38:39]
	v_pk_add_f32 v[20:21], v[20:21], v[40:41]
	v_pk_add_f32 v[14:15], v[14:15], v[34:35]
	v_pk_add_f32 v[16:17], v[16:17], v[36:37]
	v_pk_add_f32 v[6:7], v[6:7], v[34:35]
	v_pk_add_f32 v[8:9], v[8:9], v[36:37]
	v_pk_mul_f32 v[34:35], v[124:125], v[28:29]
	v_pk_mul_f32 v[36:37], v[122:123], v[26:27]
	v_pk_mul_f32 v[42:43], v[128:129], v[28:29]
	v_pk_mul_f32 v[44:45], v[126:127], v[26:27]
	v_pk_mul_f32 v[58:59], v[108:109], v[12:13]
	v_pk_mul_f32 v[60:61], v[106:107], v[10:11]
	v_pk_mul_f32 v[46:47], v[112:113], v[20:21]
	v_pk_mul_f32 v[48:49], v[110:111], v[18:19]
	v_pk_mul_f32 v[50:51], v[120:121], v[20:21]
	v_pk_mul_f32 v[52:53], v[118:119], v[18:19]
	v_pk_fma_f32 v[36:37], v[126:127], v[30:31], v[36:37] neg_lo:[0,0,1] neg_hi:[0,0,1]
	v_pk_fma_f32 v[34:35], v[128:129], v[32:33], v[34:35] neg_lo:[0,0,1] neg_hi:[0,0,1]
	v_pk_fma_f32 v[44:45], v[122:123], v[30:31], v[44:45]
	v_pk_fma_f32 v[42:43], v[124:125], v[32:33], v[42:43]
	v_pk_fma_f32 v[60:61], v[114:115], v[14:15], v[60:61]
	v_pk_fma_f32 v[58:59], v[116:117], v[16:17], v[58:59]
	v_pk_mul_f32 v[54:55], v[116:117], v[12:13]
	v_pk_mul_f32 v[56:57], v[114:115], v[10:11]
	v_pk_fma_f32 v[48:49], v[118:119], v[22:23], v[48:49] neg_lo:[0,0,1] neg_hi:[0,0,1]
	v_pk_fma_f32 v[46:47], v[120:121], v[24:25], v[46:47] neg_lo:[0,0,1] neg_hi:[0,0,1]
	v_pk_fma_f32 v[52:53], v[110:111], v[22:23], v[52:53]
	v_pk_fma_f32 v[50:51], v[112:113], v[24:25], v[50:51]
	v_cndmask_b32_e64 v32, v32, v34, s[6:7]
	v_cndmask_b32_e64 v33, v33, v35, s[6:7]
	v_cndmask_b32_e64 v30, v30, v36, s[6:7]
	v_cndmask_b32_e64 v31, v31, v37, s[6:7]
	v_cndmask_b32_e64 v28, v28, v42, s[6:7]
	v_cndmask_b32_e64 v29, v29, v43, s[6:7]
	v_cndmask_b32_e64 v26, v26, v44, s[6:7]
	v_cndmask_b32_e64 v27, v27, v45, s[6:7]
	v_cndmask_b32_e64 v34, v12, v58, s[6:7]
	v_cndmask_b32_e64 v35, v13, v59, s[6:7]
	v_cndmask_b32_e64 v36, v10, v60, s[6:7]
	v_cndmask_b32_e64 v37, v11, v61, s[6:7]
	v_cvt_pk_f16_f32 v10, v30, v31
	v_cvt_pk_f16_f32 v11, v32, v33
	v_cvt_pk_f16_f32 v12, v26, v27
	v_cvt_pk_f16_f32 v13, v28, v29
	v_pk_fma_f32 v[56:57], v[106:107], v[14:15], v[56:57] neg_lo:[0,0,1] neg_hi:[0,0,1]
	v_pk_fma_f32 v[54:55], v[108:109], v[16:17], v[54:55] neg_lo:[0,0,1] neg_hi:[0,0,1]
	v_cndmask_b32_e64 v24, v24, v46, s[6:7]
	v_cndmask_b32_e64 v25, v25, v47, s[6:7]
	v_cndmask_b32_e64 v22, v22, v48, s[6:7]
	v_cndmask_b32_e64 v23, v23, v49, s[6:7]
	v_cndmask_b32_e64 v20, v20, v50, s[6:7]
	v_cndmask_b32_e64 v21, v21, v51, s[6:7]
	v_cndmask_b32_e64 v18, v18, v52, s[6:7]
	v_cndmask_b32_e64 v19, v19, v53, s[6:7]
	ds_write_b64 v62, v[10:11]
	ds_write_b64 v63, v[12:13]
	v_cvt_pk_f16_f32 v10, v22, v23
	v_cvt_pk_f16_f32 v11, v24, v25
	v_cvt_pk_f16_f32 v12, v18, v19
	v_cvt_pk_f16_f32 v13, v20, v21
	v_cndmask_b32_e64 v16, v16, v54, s[6:7]
	v_cndmask_b32_e64 v17, v17, v55, s[6:7]
	v_cndmask_b32_e64 v14, v14, v56, s[6:7]
	v_cndmask_b32_e64 v15, v15, v57, s[6:7]
	ds_write_b64 v64, v[10:11]
	ds_write_b64 v65, v[12:13]
	v_cvt_pk_f16_f32 v10, v14, v15
	v_cvt_pk_f16_f32 v11, v16, v17
	v_cvt_pk_f16_f32 v12, v36, v37
	v_cvt_pk_f16_f32 v13, v34, v35
	v_pk_add_f32 v[2:3], v[2:3], v[38:39]
	v_pk_add_f32 v[4:5], v[4:5], v[40:41]
	ds_write_b64 v66, v[10:11]
	ds_write_b64 v67, v[12:13]
	v_pk_mul_f32 v[10:11], v[100:101], v[4:5]
	v_pk_mul_f32 v[12:13], v[98:99], v[2:3]
	v_pk_mul_f32 v[14:15], v[104:105], v[4:5]
	v_pk_mul_f32 v[16:17], v[102:103], v[2:3]
	v_pk_fma_f32 v[12:13], v[102:103], v[6:7], v[12:13] neg_lo:[0,0,1] neg_hi:[0,0,1]
	v_pk_fma_f32 v[10:11], v[104:105], v[8:9], v[10:11] neg_lo:[0,0,1] neg_hi:[0,0,1]
	v_pk_fma_f32 v[16:17], v[98:99], v[6:7], v[16:17]
	v_pk_fma_f32 v[14:15], v[100:101], v[8:9], v[14:15]
	v_cndmask_b32_e64 v8, v8, v10, s[6:7]
	v_cndmask_b32_e64 v6, v6, v12, s[6:7]
	v_cndmask_b32_e64 v7, v7, v13, s[6:7]
	v_cndmask_b32_e64 v10, v4, v14, s[6:7]
	v_cndmask_b32_e64 v5, v5, v15, s[6:7]
	v_cndmask_b32_e64 v4, v2, v16, s[6:7]
	v_add_u32_e32 v12, 0x14300, v131
	v_cvt_pk_f16_f32 v2, v6, v7
	v_cndmask_b32_e64 v9, v9, v11, s[6:7]
	v_cndmask_b32_e64 v11, v3, v17, s[6:7]
	v_cvt_pk_f16_f32 v3, v8, v9
	v_cvt_pk_f16_f32 v4, v4, v11
	v_cvt_pk_f16_f32 v5, v10, v5
	ds_write_b64 v12, v[2:3]
	v_add_u32_e32 v2, 0x14380, v131
	ds_write_b64 v2, v[4:5]
	v_lshrrev_b32_e32 v2, 5, v0
	v_and_b32_e32 v9, 4, v2
	v_lshlrev_b32_e32 v2, 3, v0
	v_and_b32_e32 v6, 0x60, v2
	v_and_b32_e32 v2, 0xf0, v132
	v_add_u32_e32 v8, 0, v2
	v_and_b32_e32 v2, 0x7f, v0
	v_or_b32_e32 v4, s29, v2
	v_and_b32_e32 v7, 3, v0
	v_add_u32_e32 v3, 0, v130
	v_lshrrev_b32_e32 v11, 1, v4
	v_lshrrev_b32_e32 v5, 4, v0
	v_bfe_u32 v10, v0, 4, 2
	v_bfe_u32 v4, v0, 4, 4
	s_mov_b64 s[6:7], -1
	s_waitcnt lgkmcnt(0)
	s_barrier
	s_cbranch_vccz .LBB2_39
	s_cmp_gt_u32 s31, 19
	s_mov_b64 s[0:1], -1
	s_cbranch_scc0 .LBB2_36
	s_sub_i32 s6, s31, 20
	s_and_b32 s0, s2, 4
	s_add_i32 s0, s6, s0
	v_and_b32_e32 v12, 16, v5
	v_lshlrev_b32_e32 v13, 1, v5
	s_ashr_i32 s1, s0, 31
	v_and_or_b32 v12, v13, 8, v12
	s_movk_i32 s7, 0x110
	s_lshl_b64 s[0:1], s[0:1], 19
	v_lshlrev_b32_e32 v16, 4, v12
	v_or_b32_e32 v12, v10, v9
	v_mad_u32_u24 v17, v5, s7, v8
	s_add_u32 s0, s12, s0
	v_lshlrev_b32_e32 v28, 2, v12
	ds_read_b128 v[12:15], v17
	s_addc_u32 s1, s13, s1
	s_lshl_b32 s14, s3, 11
	s_and_b32 s14, s14, 0x7800
	v_or3_b32 v16, v16, s14, v7
	v_or3_b32 v29, v16, v6, v28
	v_lshlrev_b32_e32 v20, 4, v29
	s_waitcnt lgkmcnt(0)
	global_store_dwordx4 v20, v[12:15], s[0:1] sc1
	v_lshrrev_b32_e32 v21, 3, v0
	ds_read_b128 v[16:19], v17 offset:17408
	v_or_b32_e32 v12, 0x200, v0
	v_lshrrev_b32_e32 v12, 4, v12
	v_and_b32_e32 v20, 48, v12
	v_mad_u32_u24 v12, v12, s7, v8
	ds_read_b128 v[12:15], v12
	s_and_b32 s15, s29, 0x7c0
	v_and_b32_e32 v30, 8, v21
	v_or3_b32 v20, v20, v30, s15
	v_lshl_or_b32 v20, v20, 4, v6
	v_or3_b32 v24, v20, v28, v7
	v_mov_b32_e32 v25, 0
	v_or_b32_e32 v20, 0x600, v0
	v_lshl_add_u64 v[26:27], v[24:25], 4, s[0:1]
	v_lshrrev_b32_e32 v31, 4, v20
	v_or_b32_e32 v24, 0x400, v29
	s_waitcnt lgkmcnt(0)
	global_store_dwordx4 v[26:27], v[12:15], off sc1
	v_mad_u32_u24 v20, v31, s7, v8
	s_movk_i32 s14, 0x7c0
	v_lshl_add_u64 v[12:13], v[24:25], 4, s[0:1]
	v_add_u32_e32 v14, s29, v31
	global_store_dwordx4 v[12:13], v[16:19], off sc1
	v_lshrrev_b32_e32 v12, 9, v14
	v_and_b32_e32 v12, 12, v12
	ds_read_b128 v[20:23], v20
	v_and_or_b32 v15, v31, 48, v30
	v_add_u32_e32 v12, s6, v12
	v_ashrrev_i32_e32 v13, 31, v12
	v_and_or_b32 v14, v14, s14, v15
	v_lshlrev_b64 v[12:13], 19, v[12:13]
	v_lshl_or_b32 v14, v14, 4, v6
	v_lshl_add_u64 v[12:13], s[12:13], 0, v[12:13]
	v_or3_b32 v24, v14, v28, v7
	v_lshl_add_u64 v[12:13], v[24:25], 4, v[12:13]
	s_waitcnt lgkmcnt(0)
	global_store_dwordx4 v[12:13], v[20:23], off sc1
	s_mov_b64 s[0:1], 0
